# v_AB without the 33 compiler pad s_nop 0 between accumulate-chain MFMA groups (int8 K-loops)
# baseline (speedup 1.0000x reference)
.LBB0_216:
	v_add_u32_e32 v130, s88, v196
	v_add_u32_e32 v134, s89, v196
	ds_read_b128 v[158:161], v130
	ds_read_b128 v[150:153], v130 offset:1024
	ds_read_b128 v[154:157], v130 offset:2048
	ds_read_b128 v[146:149], v130 offset:3072
	ds_read_b128 v[142:145], v134
	ds_read_b128 v[130:133], v134 offset:1024
	ds_read_b128 v[138:141], v134 offset:2048
	ds_read_b128 v[134:137], v134 offset:3072
	s_add_u32 s25, s50, 0xfff80080
	s_addc_u32 s56, s51, -1
	s_and_b64 s[18:19], s[18:19], exec
	s_cselect_b32 s59, s31, s56
	s_cselect_b32 s58, s4, s25
	s_cselect_b32 s57, s5, s64
	s_cselect_b32 s56, s29, s92
	s_add_i32 m0, s39, 0xc000
	ds_read_b128 v[186:189], v198
	ds_read_b128 v[190:193], v198 offset:1024
	ds_read_b128 v[200:203], v198 offset:2048
	ds_read_b128 v[204:207], v198 offset:3072
	ds_read_b128 v[208:211], v198 offset:4096
	ds_read_b128 v[212:215], v198 offset:5120
	ds_read_b128 v[216:219], v198 offset:6144
	ds_read_b128 v[220:223], v198 offset:7168
	global_load_lds_dwordx4 v170, s[50:51]
	s_add_i32 m0, s39, 0xe000
	s_nop 0
	global_load_lds_dwordx4 v172, s[50:51]
	s_waitcnt vmcnt(8) lgkmcnt(0)
	s_barrier
	s_setprio 1
	v_mfma_i32_16x16x64_i8 v[126:129], v[158:161], v[186:189], v[126:129]
	v_mfma_i32_16x16x64_i8 v[122:125], v[154:157], v[186:189], v[122:125]
	v_mfma_i32_16x16x64_i8 v[106:109], v[154:157], v[200:203], v[106:109]
	v_mfma_i32_16x16x64_i8 v[110:113], v[158:161], v[200:203], v[110:113]
	v_mfma_i32_16x16x64_i8 v[94:97], v[158:161], v[208:211], v[94:97]
	v_mfma_i32_16x16x64_i8 v[90:93], v[154:157], v[208:211], v[90:93]
	v_mfma_i32_16x16x64_i8 v[74:77], v[154:157], v[216:219], v[74:77]
	v_mfma_i32_16x16x64_i8 v[78:81], v[158:161], v[216:219], v[78:81]
	v_mfma_i32_16x16x64_i8 v[126:129], v[150:153], v[190:193], v[126:129]
	v_mfma_i32_16x16x64_i8 v[122:125], v[146:149], v[190:193], v[122:125]
	v_mfma_i32_16x16x64_i8 v[106:109], v[146:149], v[204:207], v[106:109]
	v_mfma_i32_16x16x64_i8 v[110:113], v[150:153], v[204:207], v[110:113]
	v_mfma_i32_16x16x64_i8 v[94:97], v[150:153], v[212:215], v[94:97]
	v_mfma_i32_16x16x64_i8 v[90:93], v[146:149], v[212:215], v[90:93]
	v_mfma_i32_16x16x64_i8 v[74:77], v[146:149], v[220:223], v[74:77]
	v_mfma_i32_16x16x64_i8 v[78:81], v[150:153], v[220:223], v[78:81]
	v_mfma_i32_16x16x64_i8 v[118:121], v[142:145], v[186:189], v[118:121]
	v_mfma_i32_16x16x64_i8 v[114:117], v[138:141], v[186:189], v[114:117]
	v_mfma_i32_16x16x64_i8 v[98:101], v[138:141], v[200:203], v[98:101]
	v_mfma_i32_16x16x64_i8 v[102:105], v[142:145], v[200:203], v[102:105]
	v_mfma_i32_16x16x64_i8 v[86:89], v[142:145], v[208:211], v[86:89]
	v_mfma_i32_16x16x64_i8 v[82:85], v[138:141], v[208:211], v[82:85]
	v_mfma_i32_16x16x64_i8 v[66:69], v[138:141], v[216:219], v[66:69]
	v_mfma_i32_16x16x64_i8 v[70:73], v[142:145], v[216:219], v[70:73]
	v_mfma_i32_16x16x64_i8 v[118:121], v[130:133], v[190:193], v[118:121]
	v_mfma_i32_16x16x64_i8 v[114:117], v[134:137], v[190:193], v[114:117]
	v_mfma_i32_16x16x64_i8 v[98:101], v[134:137], v[204:207], v[98:101]
	v_mfma_i32_16x16x64_i8 v[102:105], v[130:133], v[204:207], v[102:105]
	v_mfma_i32_16x16x64_i8 v[86:89], v[130:133], v[212:215], v[86:89]
	v_mfma_i32_16x16x64_i8 v[82:85], v[134:137], v[212:215], v[82:85]
	v_mfma_i32_16x16x64_i8 v[66:69], v[134:137], v[220:223], v[66:69]
	v_mfma_i32_16x16x64_i8 v[70:73], v[130:133], v[220:223], v[70:73]
	s_setprio 0
	s_barrier
	s_add_i32 s18, s88, s7
	s_mov_b32 m0, s18
	ds_read_b128 v[200:203], v198 offset:16384
	ds_read_b128 v[204:207], v198 offset:17408
	ds_read_b128 v[208:211], v198 offset:18432
	ds_read_b128 v[212:215], v198 offset:19456
	ds_read_b128 v[216:219], v198 offset:20480
	ds_read_b128 v[220:223], v198 offset:21504
	ds_read_b128 v[224:227], v198 offset:22528
	ds_read_b128 v[228:231], v198 offset:23552
	global_load_lds_dwordx4 v164, s[56:57]
	s_add_i32 m0, s18, 0x2000
	s_add_u32 s18, s56, 0x80000
	s_addc_u32 s19, s57, 0
	s_add_i32 s25, s89, s7
	global_load_lds_dwordx4 v168, s[56:57]
	s_mov_b32 m0, s25
	s_nop 0
	global_load_lds_dwordx4 v164, s[18:19]
	s_add_i32 m0, s25, 0x2000
	s_nop 0
	global_load_lds_dwordx4 v168, s[18:19]
	s_mov_b32 m0, s39
	s_nop 0
	global_load_lds_dwordx4 v162, s[58:59]
	s_mov_b32 m0, s43
	s_nop 0
	global_load_lds_dwordx4 v166, s[58:59]
	s_waitcnt vmcnt(8) lgkmcnt(0)
	s_barrier
	s_setprio 1
	v_mfma_i32_16x16x64_i8 v[62:65], v[158:161], v[200:203], v[62:65]
	v_mfma_i32_16x16x64_i8 v[58:61], v[154:157], v[200:203], v[58:61]
	v_mfma_i32_16x16x64_i8 v[42:45], v[154:157], v[208:211], v[42:45]
	v_mfma_i32_16x16x64_i8 v[46:49], v[158:161], v[208:211], v[46:49]
	v_mfma_i32_16x16x64_i8 v[30:33], v[158:161], v[216:219], v[30:33]
	v_mfma_i32_16x16x64_i8 v[26:29], v[154:157], v[216:219], v[26:29]
	v_mfma_i32_16x16x64_i8 v[10:13], v[154:157], v[224:227], v[10:13]
	v_mfma_i32_16x16x64_i8 v[14:17], v[158:161], v[224:227], v[14:17]
	v_mfma_i32_16x16x64_i8 v[62:65], v[150:153], v[204:207], v[62:65]
	v_mfma_i32_16x16x64_i8 v[58:61], v[146:149], v[204:207], v[58:61]
	v_mfma_i32_16x16x64_i8 v[42:45], v[146:149], v[212:215], v[42:45]
	v_mfma_i32_16x16x64_i8 v[46:49], v[150:153], v[212:215], v[46:49]
	v_mfma_i32_16x16x64_i8 v[30:33], v[150:153], v[220:223], v[30:33]
	v_mfma_i32_16x16x64_i8 v[26:29], v[146:149], v[220:223], v[26:29]
	v_mfma_i32_16x16x64_i8 v[10:13], v[146:149], v[228:231], v[10:13]
	v_mfma_i32_16x16x64_i8 v[14:17], v[150:153], v[228:231], v[14:17]
	v_mfma_i32_16x16x64_i8 v[54:57], v[142:145], v[200:203], v[54:57]
	v_mfma_i32_16x16x64_i8 v[50:53], v[138:141], v[200:203], v[50:53]
	v_mfma_i32_16x16x64_i8 v[34:37], v[138:141], v[208:211], v[34:37]
	v_mfma_i32_16x16x64_i8 v[38:41], v[142:145], v[208:211], v[38:41]
	v_mfma_i32_16x16x64_i8 v[22:25], v[142:145], v[216:219], v[22:25]
	v_mfma_i32_16x16x64_i8 v[18:21], v[138:141], v[216:219], v[18:21]
	v_mfma_i32_16x16x64_i8 v[2:5], v[138:141], v[224:227], v[2:5]
	v_mfma_i32_16x16x64_i8 v[6:9], v[142:145], v[224:227], v[6:9]
	v_mfma_i32_16x16x64_i8 v[54:57], v[130:133], v[204:207], v[54:57]
	v_mfma_i32_16x16x64_i8 v[50:53], v[134:137], v[204:207], v[50:53]
	v_mfma_i32_16x16x64_i8 v[34:37], v[134:137], v[212:215], v[34:37]
	v_mfma_i32_16x16x64_i8 v[38:41], v[130:133], v[212:215], v[38:41]
	v_mfma_i32_16x16x64_i8 v[22:25], v[130:133], v[220:223], v[22:25]
	v_mfma_i32_16x16x64_i8 v[18:21], v[134:137], v[220:223], v[18:21]
	v_mfma_i32_16x16x64_i8 v[2:5], v[134:137], v[228:231], v[2:5]
	v_mfma_i32_16x16x64_i8 v[6:9], v[130:133], v[228:231], v[6:9]
	s_setprio 0
	s_barrier
	s_add_i32 s25, 0, 0x18000
	s_add_i32 vcc_lo, 0, 0x1c000
	v_add_u32_e32 v142, s25, v196
	v_add_u32_e32 v158, vcc_lo, v196
	ds_read_b128 v[130:133], v142
	ds_read_b128 v[134:137], v142 offset:1024
	ds_read_b128 v[138:141], v142 offset:2048
	ds_read_b128 v[142:145], v142 offset:3072
	ds_read_b128 v[146:149], v158
	ds_read_b128 v[150:153], v158 offset:1024
	ds_read_b128 v[154:157], v158 offset:2048
	ds_read_b128 v[158:161], v158 offset:3072
	s_add_u32 s18, s58, 0x80000
	s_addc_u32 s19, s59, 0
	s_mov_b32 m0, s61
	ds_read_b128 v[200:203], v198 offset:32768
	ds_read_b128 v[204:207], v198 offset:33792
	ds_read_b128 v[208:211], v198 offset:34816
	ds_read_b128 v[212:215], v198 offset:35840
	ds_read_b128 v[216:219], v198 offset:36864
	ds_read_b128 v[220:223], v198 offset:37888
	ds_read_b128 v[224:227], v198 offset:38912
	ds_read_b128 v[228:231], v198 offset:39936
	global_load_lds_dwordx4 v162, s[18:19]
	s_mov_b32 m0, s62
	s_nop 0
	global_load_lds_dwordx4 v166, s[18:19]
	s_waitcnt vmcnt(8) lgkmcnt(0)
	s_barrier
	s_setprio 1
	v_mfma_i32_16x16x64_i8 v[126:129], v[130:133], v[200:203], v[126:129]
	v_mfma_i32_16x16x64_i8 v[122:125], v[138:141], v[200:203], v[122:125]
	v_mfma_i32_16x16x64_i8 v[106:109], v[138:141], v[208:211], v[106:109]
	v_mfma_i32_16x16x64_i8 v[110:113], v[130:133], v[208:211], v[110:113]
	v_mfma_i32_16x16x64_i8 v[94:97], v[130:133], v[216:219], v[94:97]
	v_mfma_i32_16x16x64_i8 v[90:93], v[138:141], v[216:219], v[90:93]
	v_mfma_i32_16x16x64_i8 v[74:77], v[138:141], v[224:227], v[74:77]
	v_mfma_i32_16x16x64_i8 v[78:81], v[130:133], v[224:227], v[78:81]
	v_mfma_i32_16x16x64_i8 v[126:129], v[134:137], v[204:207], v[126:129]
	v_mfma_i32_16x16x64_i8 v[122:125], v[142:145], v[204:207], v[122:125]
	v_mfma_i32_16x16x64_i8 v[106:109], v[142:145], v[212:215], v[106:109]
	v_mfma_i32_16x16x64_i8 v[110:113], v[134:137], v[212:215], v[110:113]
	v_mfma_i32_16x16x64_i8 v[94:97], v[134:137], v[220:223], v[94:97]
	v_mfma_i32_16x16x64_i8 v[90:93], v[142:145], v[220:223], v[90:93]
	v_mfma_i32_16x16x64_i8 v[74:77], v[142:145], v[228:231], v[74:77]
	v_mfma_i32_16x16x64_i8 v[78:81], v[134:137], v[228:231], v[78:81]
	v_mfma_i32_16x16x64_i8 v[118:121], v[146:149], v[200:203], v[118:121]
	v_mfma_i32_16x16x64_i8 v[114:117], v[154:157], v[200:203], v[114:117]
	v_mfma_i32_16x16x64_i8 v[98:101], v[154:157], v[208:211], v[98:101]
	v_mfma_i32_16x16x64_i8 v[102:105], v[146:149], v[208:211], v[102:105]
	v_mfma_i32_16x16x64_i8 v[86:89], v[146:149], v[216:219], v[86:89]
	v_mfma_i32_16x16x64_i8 v[82:85], v[154:157], v[216:219], v[82:85]
	v_mfma_i32_16x16x64_i8 v[66:69], v[154:157], v[224:227], v[66:69]
	v_mfma_i32_16x16x64_i8 v[70:73], v[146:149], v[224:227], v[70:73]
	v_mfma_i32_16x16x64_i8 v[118:121], v[150:153], v[204:207], v[118:121]
	v_mfma_i32_16x16x64_i8 v[114:117], v[158:161], v[204:207], v[114:117]
	v_mfma_i32_16x16x64_i8 v[98:101], v[158:161], v[212:215], v[98:101]
	v_mfma_i32_16x16x64_i8 v[102:105], v[150:153], v[212:215], v[102:105]
	v_mfma_i32_16x16x64_i8 v[86:89], v[150:153], v[220:223], v[86:89]
	v_mfma_i32_16x16x64_i8 v[82:85], v[158:161], v[220:223], v[82:85]
	v_mfma_i32_16x16x64_i8 v[66:69], v[158:161], v[228:231], v[66:69]
	v_mfma_i32_16x16x64_i8 v[70:73], v[150:153], v[228:231], v[70:73]
	s_setprio 0
	s_barrier
	s_add_i32 s18, s25, s7
	s_mov_b32 m0, s18
	s_add_u32 s98, s56, 0x80
	s_addc_u32 s99, s57, 0
	s_add_u32 s100, s58, 0x80
	s_addc_u32 s101, s59, 0
	ds_read_b128 v[200:203], v198 offset:49152
	ds_read_b128 v[204:207], v198 offset:50176
	ds_read_b128 v[208:211], v198 offset:51200
	ds_read_b128 v[212:215], v198 offset:52224
	ds_read_b128 v[216:219], v198 offset:53248
	ds_read_b128 v[220:223], v198 offset:54272
	ds_read_b128 v[224:227], v198 offset:55296
	ds_read_b128 v[228:231], v198 offset:56320
	global_load_lds_dwordx4 v164, s[98:99]
	s_add_i32 m0, s18, 0x2000
	s_add_u32 s18, s56, 0x80080
	s_addc_u32 s19, s57, 0
	s_add_i32 s25, vcc_lo, s7
	global_load_lds_dwordx4 v168, s[98:99]
	s_mov_b32 m0, s25
	s_nop 0
	global_load_lds_dwordx4 v164, s[18:19]
	s_add_i32 m0, s25, 0x2000
	s_nop 0
	global_load_lds_dwordx4 v168, s[18:19]
	s_mov_b32 m0, s67
	s_nop 0
	global_load_lds_dwordx4 v162, s[100:101]
	s_mov_b32 m0, s68
	s_nop 0
	global_load_lds_dwordx4 v166, s[100:101]
	s_waitcnt vmcnt(8) lgkmcnt(0)
	s_barrier
	s_setprio 1
	v_mfma_i32_16x16x64_i8 v[62:65], v[130:133], v[200:203], v[62:65]
	v_mfma_i32_16x16x64_i8 v[58:61], v[138:141], v[200:203], v[58:61]
	v_mfma_i32_16x16x64_i8 v[42:45], v[138:141], v[208:211], v[42:45]
	v_mfma_i32_16x16x64_i8 v[46:49], v[130:133], v[208:211], v[46:49]
	v_mfma_i32_16x16x64_i8 v[30:33], v[130:133], v[216:219], v[30:33]
	v_mfma_i32_16x16x64_i8 v[26:29], v[138:141], v[216:219], v[26:29]
	v_mfma_i32_16x16x64_i8 v[10:13], v[138:141], v[224:227], v[10:13]
	v_mfma_i32_16x16x64_i8 v[14:17], v[130:133], v[224:227], v[14:17]
	v_mfma_i32_16x16x64_i8 v[62:65], v[134:137], v[204:207], v[62:65]
	v_mfma_i32_16x16x64_i8 v[58:61], v[142:145], v[204:207], v[58:61]
	v_mfma_i32_16x16x64_i8 v[42:45], v[142:145], v[212:215], v[42:45]
	v_mfma_i32_16x16x64_i8 v[46:49], v[134:137], v[212:215], v[46:49]
	v_mfma_i32_16x16x64_i8 v[30:33], v[134:137], v[220:223], v[30:33]
	v_mfma_i32_16x16x64_i8 v[26:29], v[142:145], v[220:223], v[26:29]
	v_mfma_i32_16x16x64_i8 v[10:13], v[142:145], v[228:231], v[10:13]
	v_mfma_i32_16x16x64_i8 v[14:17], v[134:137], v[228:231], v[14:17]
	v_mfma_i32_16x16x64_i8 v[54:57], v[146:149], v[200:203], v[54:57]
	v_mfma_i32_16x16x64_i8 v[50:53], v[154:157], v[200:203], v[50:53]
	v_mfma_i32_16x16x64_i8 v[34:37], v[154:157], v[208:211], v[34:37]
	v_mfma_i32_16x16x64_i8 v[38:41], v[146:149], v[208:211], v[38:41]
	v_mfma_i32_16x16x64_i8 v[22:25], v[146:149], v[216:219], v[22:25]
	v_mfma_i32_16x16x64_i8 v[18:21], v[154:157], v[216:219], v[18:21]
	v_mfma_i32_16x16x64_i8 v[2:5], v[154:157], v[224:227], v[2:5]
	v_mfma_i32_16x16x64_i8 v[6:9], v[146:149], v[224:227], v[6:9]
	v_mfma_i32_16x16x64_i8 v[54:57], v[150:153], v[204:207], v[54:57]
	v_mfma_i32_16x16x64_i8 v[50:53], v[158:161], v[204:207], v[50:53]
	v_mfma_i32_16x16x64_i8 v[34:37], v[158:161], v[212:215], v[34:37]
	v_mfma_i32_16x16x64_i8 v[38:41], v[150:153], v[212:215], v[38:41]
	v_mfma_i32_16x16x64_i8 v[22:25], v[150:153], v[220:223], v[22:25]
	v_mfma_i32_16x16x64_i8 v[18:21], v[158:161], v[220:223], v[18:21]
	v_mfma_i32_16x16x64_i8 v[2:5], v[158:161], v[228:231], v[2:5]
	v_mfma_i32_16x16x64_i8 v[6:9], v[150:153], v[228:231], v[6:9]
	s_setprio 0
	s_barrier
	s_add_i32 s65, s65, 2
	s_add_u32 s50, s50, 0x100
	s_addc_u32 s51, s51, 0
	s_add_u32 s92, s92, 0x100
	s_addc_u32 s64, s64, 0
	s_cmp_gt_u32 s65, 29
	s_cbranch_scc1 .LBB0_219

.LBB0_702:
	v_add_u32_e32 v34, s0, v46
	s_mov_b32 s1, 0x9000
	v_mad_i64_i32 v[42:43], s[64:65], v34, s1, v[48:49]
	global_load_dwordx4 v[60:63], v[42:43], off offset:16
	global_load_dwordx4 v[64:67], v[42:43], off
	global_load_dwordx4 v[68:71], v[42:43], off offset:144
	global_load_dwordx4 v[72:75], v[42:43], off offset:128
	global_load_dwordx4 v[76:79], v[42:43], off offset:272
	global_load_dwordx4 v[80:83], v[42:43], off offset:256
	global_load_dwordx4 v[84:87], v[42:43], off offset:400
	global_load_dwordx4 v[88:91], v[42:43], off offset:384
	s_add_i32 s0, s0, 16
	s_cmpk_lg_i32 s0, 0x80
	s_waitcnt vmcnt(6)
	v_bfe_u32 v44, v64, 16, 1
	v_add3_u32 v38, v64, v44, s6
	v_bfe_u32 v44, v65, 16, 1
	v_lshrrev_b32_e32 v38, 16, v38
	v_add3_u32 v39, v65, v44, s6
	v_and_or_b32 v38, v39, s7, v38
	v_bfe_u32 v39, v66, 16, 1
	v_add3_u32 v39, v66, v39, s6
	v_bfe_u32 v40, v67, 16, 1
	v_lshrrev_b32_e32 v39, 16, v39
	v_add3_u32 v40, v67, v40, s6
	v_and_or_b32 v39, v40, s7, v39
	v_bfe_u32 v40, v60, 16, 1
	v_add3_u32 v34, v60, v40, s6
	v_bfe_u32 v40, v61, 16, 1
	v_lshrrev_b32_e32 v34, 16, v34
	v_add3_u32 v35, v61, v40, s6
	v_and_or_b32 v40, v35, s7, v34
	v_bfe_u32 v34, v62, 16, 1
	v_add3_u32 v34, v62, v34, s6
	v_bfe_u32 v35, v63, 16, 1
	v_lshrrev_b32_e32 v34, 16, v34
	v_add3_u32 v35, v63, v35, s6
	v_and_or_b32 v41, v35, s7, v34
	s_nop 1
	v_mfma_f32_16x16x32_bf16 v[34:37], v[38:41], v[2:5], 0
	v_mfma_f32_16x16x32_bf16 v[34:37], v[38:41], v[6:9], v[34:37]
	s_waitcnt vmcnt(4)
	v_bfe_u32 v44, v72, 16, 1
	v_add3_u32 v44, v72, v44, s6
	v_bfe_u32 v45, v73, 16, 1
	v_lshrrev_b32_e32 v44, 16, v44
	v_add3_u32 v45, v73, v45, s6
	v_and_or_b32 v54, v45, s7, v44
	v_bfe_u32 v44, v74, 16, 1
	v_add3_u32 v44, v74, v44, s6
	v_bfe_u32 v45, v75, 16, 1
	v_lshrrev_b32_e32 v44, 16, v44
	v_add3_u32 v45, v75, v45, s6
	v_and_or_b32 v55, v45, s7, v44
	v_bfe_u32 v44, v68, 16, 1
	v_add3_u32 v38, v68, v44, s6
	v_bfe_u32 v44, v69, 16, 1
	v_lshrrev_b32_e32 v38, 16, v38
	v_add3_u32 v39, v69, v44, s6
	v_and_or_b32 v56, v39, s7, v38
	v_bfe_u32 v38, v70, 16, 1
	v_add3_u32 v38, v70, v38, s6
	v_bfe_u32 v39, v71, 16, 1
	v_lshrrev_b32_e32 v38, 16, v38
	v_add3_u32 v39, v71, v39, s6
	v_and_or_b32 v57, v39, s7, v38
	s_nop 1
	v_mfma_f32_16x16x32_bf16 v[34:37], v[54:57], v[10:13], v[34:37]
	v_mfma_f32_16x16x32_bf16 v[34:37], v[54:57], v[14:17], v[34:37]
	s_waitcnt vmcnt(2)
	v_bfe_u32 v44, v80, 16, 1
	v_add3_u32 v44, v80, v44, s6
	v_bfe_u32 v45, v81, 16, 1
	v_lshrrev_b32_e32 v44, 16, v44
	v_add3_u32 v45, v81, v45, s6
	v_and_or_b32 v54, v45, s7, v44
	v_bfe_u32 v44, v82, 16, 1
	v_add3_u32 v44, v82, v44, s6
	v_bfe_u32 v45, v83, 16, 1
	v_lshrrev_b32_e32 v44, 16, v44
	v_add3_u32 v45, v83, v45, s6
	v_and_or_b32 v55, v45, s7, v44
	v_bfe_u32 v44, v76, 16, 1
	v_add3_u32 v38, v76, v44, s6
	v_bfe_u32 v44, v77, 16, 1
	v_lshrrev_b32_e32 v38, 16, v38
	v_add3_u32 v39, v77, v44, s6
	v_and_or_b32 v56, v39, s7, v38
	v_bfe_u32 v38, v78, 16, 1
	v_add3_u32 v38, v78, v38, s6
	v_bfe_u32 v39, v79, 16, 1
	v_lshrrev_b32_e32 v38, 16, v38
	v_add3_u32 v39, v79, v39, s6
	v_and_or_b32 v57, v39, s7, v38
	s_nop 0
	v_mfma_f32_16x16x32_bf16 v[34:37], v[54:57], v[18:21], v[34:37]
	s_waitcnt vmcnt(0)
	v_bfe_u32 v53, v88, 16, 1
	v_add3_u32 v42, v88, v53, s6
	v_bfe_u32 v53, v89, 16, 1
	v_lshrrev_b32_e32 v42, 16, v42
	v_add3_u32 v43, v89, v53, s6
	v_and_or_b32 v42, v43, s7, v42
	v_bfe_u32 v43, v90, 16, 1
	v_add3_u32 v43, v90, v43, s6
	v_bfe_u32 v44, v91, 16, 1
	v_lshrrev_b32_e32 v43, 16, v43
	v_add3_u32 v44, v91, v44, s6
	v_and_or_b32 v43, v44, s7, v43
	v_bfe_u32 v44, v84, 16, 1
	v_add3_u32 v38, v84, v44, s6
	v_bfe_u32 v44, v85, 16, 1
	v_lshrrev_b32_e32 v38, 16, v38
	v_add3_u32 v39, v85, v44, s6
	v_and_or_b32 v44, v39, s7, v38
	v_bfe_u32 v38, v86, 16, 1
	v_add3_u32 v38, v86, v38, s6
	v_bfe_u32 v39, v87, 16, 1
	v_lshrrev_b32_e32 v38, 16, v38
	v_add3_u32 v39, v87, v39, s6
	v_and_or_b32 v45, v39, s7, v38
	v_mfma_f32_16x16x32_bf16 v[34:37], v[54:57], v[22:25], v[34:37]
	v_mfma_f32_16x16x32_bf16 v[34:37], v[42:45], v[26:29], v[34:37]
	v_mfma_f32_16x16x32_bf16 v[34:37], v[42:45], v[30:33], v[34:37]
	s_nop 7
	v_bfe_u32 v38, v34, 16, 1
	v_add3_u32 v34, v34, v38, s6
	v_bfe_u32 v38, v35, 16, 1
	v_lshrrev_b32_e32 v34, 16, v34
	v_add3_u32 v35, v35, v38, s6
	v_and_or_b32 v34, v35, s7, v34
	v_bfe_u32 v35, v36, 16, 1
	v_add3_u32 v35, v36, v35, s6
	v_bfe_u32 v36, v37, 16, 1
	v_lshrrev_b32_e32 v35, 16, v35
	v_add3_u32 v36, v37, v36, s6
	v_and_or_b32 v35, v36, s7, v35
	global_store_dwordx2 v[50:51], v[34:35], off
	v_lshl_add_u64 v[50:51], v[50:51], 0, 32
	s_cbranch_scc1 .LBB0_702
	s_add_i32 s60, s60, s33
	s_add_i32 s19, s19, s33
	s_cmpk_gt_i32 s60, 0xff
	s_cbranch_scc0 .LBB0_697

.LBB0_788:
	v_add_u32_e32 v130, s15, v190
	v_add_u32_e32 v134, s50, v190
	ds_read_b128 v[158:161], v130
	ds_read_b128 v[150:153], v130 offset:1024
	ds_read_b128 v[154:157], v130 offset:2048
	ds_read_b128 v[146:149], v130 offset:3072
	ds_read_b128 v[142:145], v134
	ds_read_b128 v[130:133], v134 offset:1024
	ds_read_b128 v[138:141], v134 offset:2048
	ds_read_b128 v[134:137], v134 offset:3072
	s_add_u32 s36, s34, 0xfff80080
	s_addc_u32 s37, s35, -1
	s_and_b64 s[0:1], s[0:1], exec
	s_cselect_b32 s39, s21, s37
	s_cselect_b32 s38, s60, s36
	s_cselect_b32 s37, s17, s63
	s_cselect_b32 s36, s61, s62
	s_add_i32 m0, s29, 0xc000
	ds_read_b128 v[182:185], v193
	ds_read_b128 v[186:189], v193 offset:1024
	ds_read_b128 v[194:197], v193 offset:2048
	ds_read_b128 v[198:201], v193 offset:3072
	ds_read_b128 v[202:205], v193 offset:4096
	ds_read_b128 v[206:209], v193 offset:5120
	ds_read_b128 v[210:213], v193 offset:6144
	ds_read_b128 v[214:217], v193 offset:7168
	global_load_lds_dwordx4 v172, s[34:35]
	s_add_i32 m0, s29, 0xe000
	s_nop 0
	global_load_lds_dwordx4 v174, s[34:35]
	s_waitcnt vmcnt(8) lgkmcnt(0)
	s_barrier
	s_setprio 1
	v_mfma_i32_16x16x64_i8 v[126:129], v[158:161], v[182:185], v[126:129]
	v_mfma_i32_16x16x64_i8 v[122:125], v[154:157], v[182:185], v[122:125]
	v_mfma_i32_16x16x64_i8 v[106:109], v[154:157], v[194:197], v[106:109]
	v_mfma_i32_16x16x64_i8 v[114:117], v[158:161], v[194:197], v[114:117]
	v_mfma_i32_16x16x64_i8 v[98:101], v[158:161], v[202:205], v[98:101]
	v_mfma_i32_16x16x64_i8 v[90:93], v[154:157], v[202:205], v[90:93]
	v_mfma_i32_16x16x64_i8 v[74:77], v[154:157], v[210:213], v[74:77]
	v_mfma_i32_16x16x64_i8 v[82:85], v[158:161], v[210:213], v[82:85]
	v_mfma_i32_16x16x64_i8 v[126:129], v[150:153], v[186:189], v[126:129]
	v_mfma_i32_16x16x64_i8 v[122:125], v[146:149], v[186:189], v[122:125]
	v_mfma_i32_16x16x64_i8 v[106:109], v[146:149], v[198:201], v[106:109]
	v_mfma_i32_16x16x64_i8 v[114:117], v[150:153], v[198:201], v[114:117]
	v_mfma_i32_16x16x64_i8 v[98:101], v[150:153], v[206:209], v[98:101]
	v_mfma_i32_16x16x64_i8 v[90:93], v[146:149], v[206:209], v[90:93]
	v_mfma_i32_16x16x64_i8 v[74:77], v[146:149], v[214:217], v[74:77]
	v_mfma_i32_16x16x64_i8 v[82:85], v[150:153], v[214:217], v[82:85]
	v_mfma_i32_16x16x64_i8 v[118:121], v[142:145], v[182:185], v[118:121]
	v_mfma_i32_16x16x64_i8 v[110:113], v[138:141], v[182:185], v[110:113]
	v_mfma_i32_16x16x64_i8 v[94:97], v[138:141], v[194:197], v[94:97]
	v_mfma_i32_16x16x64_i8 v[102:105], v[142:145], v[194:197], v[102:105]
	v_mfma_i32_16x16x64_i8 v[86:89], v[142:145], v[202:205], v[86:89]
	v_mfma_i32_16x16x64_i8 v[78:81], v[138:141], v[202:205], v[78:81]
	v_mfma_i32_16x16x64_i8 v[66:69], v[138:141], v[210:213], v[66:69]
	v_mfma_i32_16x16x64_i8 v[70:73], v[142:145], v[210:213], v[70:73]
	v_mfma_i32_16x16x64_i8 v[118:121], v[130:133], v[186:189], v[118:121]
	v_mfma_i32_16x16x64_i8 v[110:113], v[134:137], v[186:189], v[110:113]
	v_mfma_i32_16x16x64_i8 v[94:97], v[134:137], v[198:201], v[94:97]
	v_mfma_i32_16x16x64_i8 v[102:105], v[130:133], v[198:201], v[102:105]
	v_mfma_i32_16x16x64_i8 v[86:89], v[130:133], v[206:209], v[86:89]
	v_mfma_i32_16x16x64_i8 v[78:81], v[134:137], v[206:209], v[78:81]
	v_mfma_i32_16x16x64_i8 v[66:69], v[134:137], v[214:217], v[66:69]
	v_mfma_i32_16x16x64_i8 v[70:73], v[130:133], v[214:217], v[70:73]
	s_setprio 0
	s_barrier
	s_add_i32 s0, s15, s40
	s_mov_b32 m0, s0
	ds_read_b128 v[194:197], v193 offset:16384
	ds_read_b128 v[198:201], v193 offset:17408
	ds_read_b128 v[202:205], v193 offset:18432
	ds_read_b128 v[206:209], v193 offset:19456
	ds_read_b128 v[210:213], v193 offset:20480
	ds_read_b128 v[214:217], v193 offset:21504
	ds_read_b128 v[218:221], v193 offset:22528
	ds_read_b128 v[222:225], v193 offset:23552
	global_load_lds_dwordx4 v164, s[36:37]
	s_add_i32 m0, s0, 0x2000
	s_add_u32 s0, s36, 0x80000
	s_addc_u32 s1, s37, 0
	s_add_i32 s66, s50, s40
	global_load_lds_dwordx4 v168, s[36:37]
	s_mov_b32 m0, s66
	s_nop 0
	global_load_lds_dwordx4 v164, s[0:1]
	s_add_i32 m0, s66, 0x2000
	s_nop 0
	global_load_lds_dwordx4 v168, s[0:1]
	s_mov_b32 m0, s29
	s_nop 0
	global_load_lds_dwordx4 v162, s[38:39]
	s_mov_b32 m0, s31
	s_nop 0
	global_load_lds_dwordx4 v166, s[38:39]
	s_waitcnt vmcnt(8) lgkmcnt(0)
	s_barrier
	s_setprio 1
	v_mfma_i32_16x16x64_i8 v[62:65], v[158:161], v[194:197], v[62:65]
	v_mfma_i32_16x16x64_i8 v[58:61], v[154:157], v[194:197], v[58:61]
	v_mfma_i32_16x16x64_i8 v[42:45], v[154:157], v[202:205], v[42:45]
	v_mfma_i32_16x16x64_i8 v[50:53], v[158:161], v[202:205], v[50:53]
	v_mfma_i32_16x16x64_i8 v[34:37], v[158:161], v[210:213], v[34:37]
	v_mfma_i32_16x16x64_i8 v[26:29], v[154:157], v[210:213], v[26:29]
	v_mfma_i32_16x16x64_i8 v[10:13], v[154:157], v[218:221], v[10:13]
	v_mfma_i32_16x16x64_i8 v[18:21], v[158:161], v[218:221], v[18:21]
	v_mfma_i32_16x16x64_i8 v[62:65], v[150:153], v[198:201], v[62:65]
	v_mfma_i32_16x16x64_i8 v[58:61], v[146:149], v[198:201], v[58:61]
	v_mfma_i32_16x16x64_i8 v[42:45], v[146:149], v[206:209], v[42:45]
	v_mfma_i32_16x16x64_i8 v[50:53], v[150:153], v[206:209], v[50:53]
	v_mfma_i32_16x16x64_i8 v[34:37], v[150:153], v[214:217], v[34:37]
	v_mfma_i32_16x16x64_i8 v[26:29], v[146:149], v[214:217], v[26:29]
	v_mfma_i32_16x16x64_i8 v[10:13], v[146:149], v[222:225], v[10:13]
	v_mfma_i32_16x16x64_i8 v[18:21], v[150:153], v[222:225], v[18:21]
	v_mfma_i32_16x16x64_i8 v[54:57], v[142:145], v[194:197], v[54:57]
	v_mfma_i32_16x16x64_i8 v[46:49], v[138:141], v[194:197], v[46:49]
	v_mfma_i32_16x16x64_i8 v[30:33], v[138:141], v[202:205], v[30:33]
	v_mfma_i32_16x16x64_i8 v[38:41], v[142:145], v[202:205], v[38:41]
	v_mfma_i32_16x16x64_i8 v[22:25], v[142:145], v[210:213], v[22:25]
	v_mfma_i32_16x16x64_i8 v[14:17], v[138:141], v[210:213], v[14:17]
	v_mfma_i32_16x16x64_i8 v[2:5], v[138:141], v[218:221], v[2:5]
	v_mfma_i32_16x16x64_i8 v[6:9], v[142:145], v[218:221], v[6:9]
	v_mfma_i32_16x16x64_i8 v[54:57], v[130:133], v[198:201], v[54:57]
	v_mfma_i32_16x16x64_i8 v[46:49], v[134:137], v[198:201], v[46:49]
	v_mfma_i32_16x16x64_i8 v[30:33], v[134:137], v[206:209], v[30:33]
	v_mfma_i32_16x16x64_i8 v[38:41], v[130:133], v[206:209], v[38:41]
	v_mfma_i32_16x16x64_i8 v[22:25], v[130:133], v[214:217], v[22:25]
	v_mfma_i32_16x16x64_i8 v[14:17], v[134:137], v[214:217], v[14:17]
	v_mfma_i32_16x16x64_i8 v[2:5], v[134:137], v[222:225], v[2:5]
	v_mfma_i32_16x16x64_i8 v[6:9], v[130:133], v[222:225], v[6:9]
	s_setprio 0
	s_barrier
	s_add_i32 s66, 0, 0x18000
	s_add_i32 s67, 0, 0x1c000
	v_add_u32_e32 v142, s66, v190
	v_add_u32_e32 v158, s67, v190
	ds_read_b128 v[130:133], v142
	ds_read_b128 v[134:137], v142 offset:1024
	ds_read_b128 v[138:141], v142 offset:2048
	ds_read_b128 v[142:145], v142 offset:3072
	ds_read_b128 v[146:149], v158
	ds_read_b128 v[150:153], v158 offset:1024
	ds_read_b128 v[154:157], v158 offset:2048
	ds_read_b128 v[158:161], v158 offset:3072
	s_add_u32 s0, s38, 0x80000
	s_addc_u32 s1, s39, 0
	s_mov_b32 m0, s42
	ds_read_b128 v[194:197], v193 offset:32768
	ds_read_b128 v[198:201], v193 offset:33792
	ds_read_b128 v[202:205], v193 offset:34816
	ds_read_b128 v[206:209], v193 offset:35840
	ds_read_b128 v[210:213], v193 offset:36864
	ds_read_b128 v[214:217], v193 offset:37888
	ds_read_b128 v[218:221], v193 offset:38912
	ds_read_b128 v[222:225], v193 offset:39936
	global_load_lds_dwordx4 v162, s[0:1]
	s_mov_b32 m0, s43
	s_nop 0
	global_load_lds_dwordx4 v166, s[0:1]
	s_waitcnt vmcnt(8) lgkmcnt(0)
	s_barrier
	s_setprio 1
	v_mfma_i32_16x16x64_i8 v[126:129], v[130:133], v[194:197], v[126:129]
	v_mfma_i32_16x16x64_i8 v[122:125], v[138:141], v[194:197], v[122:125]
	v_mfma_i32_16x16x64_i8 v[106:109], v[138:141], v[202:205], v[106:109]
	v_mfma_i32_16x16x64_i8 v[114:117], v[130:133], v[202:205], v[114:117]
	v_mfma_i32_16x16x64_i8 v[98:101], v[130:133], v[210:213], v[98:101]
	v_mfma_i32_16x16x64_i8 v[90:93], v[138:141], v[210:213], v[90:93]
	v_mfma_i32_16x16x64_i8 v[74:77], v[138:141], v[218:221], v[74:77]
	v_mfma_i32_16x16x64_i8 v[82:85], v[130:133], v[218:221], v[82:85]
	v_mfma_i32_16x16x64_i8 v[126:129], v[134:137], v[198:201], v[126:129]
	v_mfma_i32_16x16x64_i8 v[122:125], v[142:145], v[198:201], v[122:125]
	v_mfma_i32_16x16x64_i8 v[106:109], v[142:145], v[206:209], v[106:109]
	v_mfma_i32_16x16x64_i8 v[114:117], v[134:137], v[206:209], v[114:117]
	v_mfma_i32_16x16x64_i8 v[98:101], v[134:137], v[214:217], v[98:101]
	v_mfma_i32_16x16x64_i8 v[90:93], v[142:145], v[214:217], v[90:93]
	v_mfma_i32_16x16x64_i8 v[74:77], v[142:145], v[222:225], v[74:77]
	v_mfma_i32_16x16x64_i8 v[82:85], v[134:137], v[222:225], v[82:85]
	v_mfma_i32_16x16x64_i8 v[118:121], v[146:149], v[194:197], v[118:121]
	v_mfma_i32_16x16x64_i8 v[110:113], v[154:157], v[194:197], v[110:113]
	v_mfma_i32_16x16x64_i8 v[94:97], v[154:157], v[202:205], v[94:97]
	v_mfma_i32_16x16x64_i8 v[102:105], v[146:149], v[202:205], v[102:105]
	v_mfma_i32_16x16x64_i8 v[86:89], v[146:149], v[210:213], v[86:89]
	v_mfma_i32_16x16x64_i8 v[78:81], v[154:157], v[210:213], v[78:81]
	v_mfma_i32_16x16x64_i8 v[66:69], v[154:157], v[218:221], v[66:69]
	v_mfma_i32_16x16x64_i8 v[70:73], v[146:149], v[218:221], v[70:73]
	v_mfma_i32_16x16x64_i8 v[118:121], v[150:153], v[198:201], v[118:121]
	v_mfma_i32_16x16x64_i8 v[110:113], v[158:161], v[198:201], v[110:113]
	v_mfma_i32_16x16x64_i8 v[94:97], v[158:161], v[206:209], v[94:97]
	v_mfma_i32_16x16x64_i8 v[102:105], v[150:153], v[206:209], v[102:105]
	v_mfma_i32_16x16x64_i8 v[86:89], v[150:153], v[214:217], v[86:89]
	v_mfma_i32_16x16x64_i8 v[78:81], v[158:161], v[214:217], v[78:81]
	v_mfma_i32_16x16x64_i8 v[66:69], v[158:161], v[222:225], v[66:69]
	v_mfma_i32_16x16x64_i8 v[70:73], v[150:153], v[222:225], v[70:73]
	s_setprio 0
	s_barrier
	s_add_i32 s0, s66, s40
	s_mov_b32 m0, s0
	s_add_u32 s98, s36, 0x80
	s_addc_u32 s99, s37, 0
	s_add_u32 s100, s38, 0x80
	s_addc_u32 s101, s39, 0
	ds_read_b128 v[194:197], v193 offset:49152
	ds_read_b128 v[198:201], v193 offset:50176
	ds_read_b128 v[202:205], v193 offset:51200
	ds_read_b128 v[206:209], v193 offset:52224
	ds_read_b128 v[210:213], v193 offset:53248
	ds_read_b128 v[214:217], v193 offset:54272
	ds_read_b128 v[218:221], v193 offset:55296
	ds_read_b128 v[222:225], v193 offset:56320
	global_load_lds_dwordx4 v164, s[98:99]
	s_add_i32 m0, s0, 0x2000
	s_add_u32 s0, s36, 0x80080
	s_addc_u32 s1, s37, 0
	s_add_i32 s36, s67, s40
	global_load_lds_dwordx4 v168, s[98:99]
	s_mov_b32 m0, s36
	s_nop 0
	global_load_lds_dwordx4 v164, s[0:1]
	s_add_i32 m0, s36, 0x2000
	s_nop 0
	global_load_lds_dwordx4 v168, s[0:1]
	s_mov_b32 m0, s48
	s_nop 0
	global_load_lds_dwordx4 v162, s[100:101]
	s_mov_b32 m0, s49
	s_nop 0
	global_load_lds_dwordx4 v166, s[100:101]
	s_waitcnt vmcnt(8) lgkmcnt(0)
	s_barrier
	s_setprio 1
	v_mfma_i32_16x16x64_i8 v[62:65], v[130:133], v[194:197], v[62:65]
	v_mfma_i32_16x16x64_i8 v[58:61], v[138:141], v[194:197], v[58:61]
	v_mfma_i32_16x16x64_i8 v[42:45], v[138:141], v[202:205], v[42:45]
	v_mfma_i32_16x16x64_i8 v[50:53], v[130:133], v[202:205], v[50:53]
	v_mfma_i32_16x16x64_i8 v[34:37], v[130:133], v[210:213], v[34:37]
	v_mfma_i32_16x16x64_i8 v[26:29], v[138:141], v[210:213], v[26:29]
	v_mfma_i32_16x16x64_i8 v[10:13], v[138:141], v[218:221], v[10:13]
	v_mfma_i32_16x16x64_i8 v[18:21], v[130:133], v[218:221], v[18:21]
	v_mfma_i32_16x16x64_i8 v[62:65], v[134:137], v[198:201], v[62:65]
	v_mfma_i32_16x16x64_i8 v[58:61], v[142:145], v[198:201], v[58:61]
	v_mfma_i32_16x16x64_i8 v[42:45], v[142:145], v[206:209], v[42:45]
	v_mfma_i32_16x16x64_i8 v[50:53], v[134:137], v[206:209], v[50:53]
	v_mfma_i32_16x16x64_i8 v[34:37], v[134:137], v[214:217], v[34:37]
	v_mfma_i32_16x16x64_i8 v[26:29], v[142:145], v[214:217], v[26:29]
	v_mfma_i32_16x16x64_i8 v[10:13], v[142:145], v[222:225], v[10:13]
	v_mfma_i32_16x16x64_i8 v[18:21], v[134:137], v[222:225], v[18:21]
	v_mfma_i32_16x16x64_i8 v[54:57], v[146:149], v[194:197], v[54:57]
	v_mfma_i32_16x16x64_i8 v[46:49], v[154:157], v[194:197], v[46:49]
	v_mfma_i32_16x16x64_i8 v[30:33], v[154:157], v[202:205], v[30:33]
	v_mfma_i32_16x16x64_i8 v[38:41], v[146:149], v[202:205], v[38:41]
	v_mfma_i32_16x16x64_i8 v[22:25], v[146:149], v[210:213], v[22:25]
	v_mfma_i32_16x16x64_i8 v[14:17], v[154:157], v[210:213], v[14:17]
	v_mfma_i32_16x16x64_i8 v[2:5], v[154:157], v[218:221], v[2:5]
	v_mfma_i32_16x16x64_i8 v[6:9], v[146:149], v[218:221], v[6:9]
	v_mfma_i32_16x16x64_i8 v[54:57], v[150:153], v[198:201], v[54:57]
	v_mfma_i32_16x16x64_i8 v[46:49], v[158:161], v[198:201], v[46:49]
	v_mfma_i32_16x16x64_i8 v[30:33], v[158:161], v[206:209], v[30:33]
	v_mfma_i32_16x16x64_i8 v[38:41], v[150:153], v[206:209], v[38:41]
	v_mfma_i32_16x16x64_i8 v[22:25], v[150:153], v[214:217], v[22:25]
	v_mfma_i32_16x16x64_i8 v[14:17], v[158:161], v[214:217], v[14:17]
	v_mfma_i32_16x16x64_i8 v[2:5], v[158:161], v[222:225], v[2:5]
	v_mfma_i32_16x16x64_i8 v[6:9], v[150:153], v[222:225], v[6:9]
	s_setprio 0
	s_barrier
	s_add_i32 s64, s64, 2
	s_add_u32 s34, s34, 0x100
	s_addc_u32 s35, s35, 0
	s_add_u32 s62, s62, 0x100
	s_addc_u32 s63, s63, 0
	s_cmp_gt_u32 s64, 29
	s_cbranch_scc1 .LBB0_791

.LBB0_1051:
	s_add_u32 s8, s17, s6
	s_addc_u32 s9, s48, s7
	s_add_u32 s8, s8, 0x32800100
	s_addc_u32 s9, s9, 0
	s_add_u32 s65, s49, s6
	s_addc_u32 s68, s50, s7
	s_add_i32 s69, 0, 0x10000
	s_cmpk_eq_i32 s6, 0xf00
	s_cselect_b32 s41, s5, s9
	s_cselect_b32 s40, s4, s8
	s_cselect_b32 s9, s21, s68
	s_cselect_b32 s8, s20, s65
	s_add_i32 s65, 0, 0x14000
	v_add_u32_e32 v130, s69, v187
	v_add_u32_e32 v134, s65, v187
	ds_read_b128 v[158:161], v130
	ds_read_b128 v[150:153], v130 offset:1024
	ds_read_b128 v[154:157], v130 offset:2048
	ds_read_b128 v[146:149], v130 offset:3072
	ds_read_b128 v[142:145], v134
	ds_read_b128 v[130:133], v134 offset:1024
	ds_read_b128 v[138:141], v134 offset:2048
	ds_read_b128 v[134:137], v134 offset:3072
	v_lshl_add_u64 v[214:215], v[168:169], 0, s[6:7]
	s_add_i32 m0, s43, 0xc000
	ds_read_b128 v[172:175], v188
	ds_read_b128 v[176:179], v188 offset:1024
	ds_read_b128 v[190:193], v188 offset:2048
	ds_read_b128 v[194:197], v188 offset:3072
	ds_read_b128 v[198:201], v188 offset:4096
	ds_read_b128 v[202:205], v188 offset:5120
	ds_read_b128 v[206:209], v188 offset:6144
	ds_read_b128 v[210:213], v188 offset:7168
	global_load_lds_dwordx4 v[214:215], off
	v_lshl_add_u64 v[214:215], v[170:171], 0, s[6:7]
	s_add_i32 m0, s43, 0xe000
	s_nop 0
	global_load_lds_dwordx4 v[214:215], off
	s_waitcnt vmcnt(8) lgkmcnt(0)
	s_barrier
	s_setprio 1
	v_mfma_i32_16x16x64_i8 v[70:73], v[158:161], v[172:175], v[70:73]
	v_mfma_i32_16x16x64_i8 v[34:37], v[154:157], v[172:175], v[34:37]
	v_mfma_i32_16x16x64_i8 v[54:57], v[154:157], v[190:193], v[54:57]
	v_mfma_i32_16x16x64_i8 v[102:105], v[158:161], v[190:193], v[102:105]
	v_mfma_i32_16x16x64_i8 v[114:117], v[158:161], v[198:201], v[114:117]
	v_mfma_i32_16x16x64_i8 v[86:89], v[154:157], v[198:201], v[86:89]
	v_mfma_i32_16x16x64_i8 v[110:113], v[154:157], v[206:209], v[110:113]
	v_mfma_i32_16x16x64_i8 v[126:129], v[158:161], v[206:209], v[126:129]
	v_mfma_i32_16x16x64_i8 v[70:73], v[150:153], v[176:179], v[70:73]
	v_mfma_i32_16x16x64_i8 v[34:37], v[146:149], v[176:179], v[34:37]
	v_mfma_i32_16x16x64_i8 v[54:57], v[146:149], v[194:197], v[54:57]
	v_mfma_i32_16x16x64_i8 v[102:105], v[150:153], v[194:197], v[102:105]
	v_mfma_i32_16x16x64_i8 v[114:117], v[150:153], v[202:205], v[114:117]
	v_mfma_i32_16x16x64_i8 v[86:89], v[146:149], v[202:205], v[86:89]
	v_mfma_i32_16x16x64_i8 v[110:113], v[146:149], v[210:213], v[110:113]
	v_mfma_i32_16x16x64_i8 v[126:129], v[150:153], v[210:213], v[126:129]
	v_mfma_i32_16x16x64_i8 v[18:21], v[142:145], v[172:175], v[18:21]
	v_mfma_i32_16x16x64_i8 v[2:5], v[138:141], v[172:175], v[2:5]
	v_mfma_i32_16x16x64_i8 v[6:9], v[138:141], v[190:193], v[6:9]
	v_mfma_i32_16x16x64_i8 v[38:41], v[142:145], v[190:193], v[38:41]
	v_mfma_i32_16x16x64_i8 v[66:69], v[142:145], v[198:201], v[66:69]
	v_mfma_i32_16x16x64_i8 v[26:29], v[138:141], v[198:201], v[26:29]
	v_mfma_i32_16x16x64_i8 v[50:53], v[138:141], v[206:209], v[50:53]
	v_mfma_i32_16x16x64_i8 v[90:93], v[142:145], v[206:209], v[90:93]
	v_mfma_i32_16x16x64_i8 v[18:21], v[130:133], v[176:179], v[18:21]
	v_mfma_i32_16x16x64_i8 v[2:5], v[134:137], v[176:179], v[2:5]
	v_mfma_i32_16x16x64_i8 v[6:9], v[134:137], v[194:197], v[6:9]
	v_mfma_i32_16x16x64_i8 v[38:41], v[130:133], v[194:197], v[38:41]
	v_mfma_i32_16x16x64_i8 v[66:69], v[130:133], v[202:205], v[66:69]
	v_mfma_i32_16x16x64_i8 v[26:29], v[134:137], v[202:205], v[26:29]
	v_mfma_i32_16x16x64_i8 v[50:53], v[134:137], v[210:213], v[50:53]
	v_mfma_i32_16x16x64_i8 v[90:93], v[130:133], v[210:213], v[90:93]
	s_setprio 0
	s_barrier
	s_add_i32 s68, s69, s42
	s_mov_b32 m0, s68
	ds_read_b128 v[190:193], v188 offset:16384
	ds_read_b128 v[194:197], v188 offset:17408
	ds_read_b128 v[198:201], v188 offset:18432
	ds_read_b128 v[202:205], v188 offset:19456
	ds_read_b128 v[206:209], v188 offset:20480
	ds_read_b128 v[210:213], v188 offset:21504
	ds_read_b128 v[214:217], v188 offset:22528
	ds_read_b128 v[218:221], v188 offset:23552
	global_load_lds_dwordx4 v162, s[8:9]
	s_add_i32 m0, s68, 0x2000
	s_add_u32 s68, s8, 0x80000
	s_addc_u32 s69, s9, 0
	s_add_i32 s65, s65, s42
	global_load_lds_dwordx4 v166, s[8:9]
	s_mov_b32 m0, s65
	s_nop 0
	global_load_lds_dwordx4 v162, s[68:69]
	s_add_i32 m0, s65, 0x2000
	s_nop 0
	global_load_lds_dwordx4 v166, s[68:69]
	s_mov_b32 m0, s43
	s_nop 0
	global_load_lds_dwordx4 v162, s[40:41]
	s_mov_b32 m0, s60
	s_nop 0
	global_load_lds_dwordx4 v166, s[40:41]
	s_waitcnt vmcnt(8) lgkmcnt(0)
	s_barrier
	s_setprio 1
	v_mfma_i32_16x16x64_i8 v[122:125], v[158:161], v[190:193], v[122:125]
	v_mfma_i32_16x16x64_i8 v[118:121], v[154:157], v[190:193], v[118:121]
	v_mfma_i32_16x16x64_i8 v[94:97], v[154:157], v[198:201], v[94:97]
	v_mfma_i32_16x16x64_i8 v[98:101], v[158:161], v[198:201], v[98:101]
	v_mfma_i32_16x16x64_i8 v[62:65], v[158:161], v[206:209], v[62:65]
	v_mfma_i32_16x16x64_i8 v[58:61], v[154:157], v[206:209], v[58:61]
	v_mfma_i32_16x16x64_i8 v[22:25], v[154:157], v[214:217], v[22:25]
	v_mfma_i32_16x16x64_i8 v[30:33], v[158:161], v[214:217], v[30:33]
	v_mfma_i32_16x16x64_i8 v[122:125], v[150:153], v[194:197], v[122:125]
	v_mfma_i32_16x16x64_i8 v[118:121], v[146:149], v[194:197], v[118:121]
	v_mfma_i32_16x16x64_i8 v[94:97], v[146:149], v[202:205], v[94:97]
	v_mfma_i32_16x16x64_i8 v[98:101], v[150:153], v[202:205], v[98:101]
	v_mfma_i32_16x16x64_i8 v[62:65], v[150:153], v[210:213], v[62:65]
	v_mfma_i32_16x16x64_i8 v[58:61], v[146:149], v[210:213], v[58:61]
	v_mfma_i32_16x16x64_i8 v[22:25], v[146:149], v[218:221], v[22:25]
	v_mfma_i32_16x16x64_i8 v[30:33], v[150:153], v[218:221], v[30:33]
	v_mfma_i32_16x16x64_i8 v[106:109], v[142:145], v[190:193], v[106:109]
	v_mfma_i32_16x16x64_i8 v[82:85], v[138:141], v[190:193], v[82:85]
	v_mfma_i32_16x16x64_i8 v[74:77], v[138:141], v[198:201], v[74:77]
	v_mfma_i32_16x16x64_i8 v[78:81], v[142:145], v[198:201], v[78:81]
	v_mfma_i32_16x16x64_i8 v[46:49], v[142:145], v[206:209], v[46:49]
	v_mfma_i32_16x16x64_i8 v[42:45], v[138:141], v[206:209], v[42:45]
	v_mfma_i32_16x16x64_i8 v[10:13], v[138:141], v[214:217], v[10:13]
	v_mfma_i32_16x16x64_i8 v[14:17], v[142:145], v[214:217], v[14:17]
	v_mfma_i32_16x16x64_i8 v[106:109], v[130:133], v[194:197], v[106:109]
	v_mfma_i32_16x16x64_i8 v[82:85], v[134:137], v[194:197], v[82:85]
	v_mfma_i32_16x16x64_i8 v[74:77], v[134:137], v[202:205], v[74:77]
	v_mfma_i32_16x16x64_i8 v[78:81], v[130:133], v[202:205], v[78:81]
	v_mfma_i32_16x16x64_i8 v[46:49], v[130:133], v[210:213], v[46:49]
	v_mfma_i32_16x16x64_i8 v[42:45], v[134:137], v[210:213], v[42:45]
	v_mfma_i32_16x16x64_i8 v[10:13], v[134:137], v[218:221], v[10:13]
	v_mfma_i32_16x16x64_i8 v[14:17], v[130:133], v[218:221], v[14:17]
	s_setprio 0
	s_barrier
	s_add_i32 s65, 0, 0x18000
	s_add_i32 s68, 0, 0x1c000
	v_add_u32_e32 v142, s65, v187
	v_add_u32_e32 v158, s68, v187
	ds_read_b128 v[130:133], v142
	ds_read_b128 v[134:137], v142 offset:1024
	ds_read_b128 v[138:141], v142 offset:2048
	ds_read_b128 v[142:145], v142 offset:3072
	ds_read_b128 v[146:149], v158
	ds_read_b128 v[150:153], v158 offset:1024
	ds_read_b128 v[154:157], v158 offset:2048
	ds_read_b128 v[158:161], v158 offset:3072
	s_add_u32 s40, s40, 0x80000
	s_addc_u32 s41, s41, 0
	s_add_u32 s100, s40, 0xfff80080
	s_addc_u32 s101, s41, -1
	s_mov_b32 m0, s61
	ds_read_b128 v[190:193], v188 offset:32768
	ds_read_b128 v[194:197], v188 offset:33792
	ds_read_b128 v[198:201], v188 offset:34816
	ds_read_b128 v[202:205], v188 offset:35840
	ds_read_b128 v[206:209], v188 offset:36864
	ds_read_b128 v[210:213], v188 offset:37888
	ds_read_b128 v[214:217], v188 offset:38912
	ds_read_b128 v[218:221], v188 offset:39936
	global_load_lds_dwordx4 v162, s[40:41]
	s_mov_b32 m0, s62
	s_nop 0
	global_load_lds_dwordx4 v166, s[40:41]
	s_waitcnt vmcnt(8) lgkmcnt(0)
	s_barrier
	s_setprio 1
	v_mfma_i32_16x16x64_i8 v[70:73], v[130:133], v[190:193], v[70:73]
	v_mfma_i32_16x16x64_i8 v[34:37], v[138:141], v[190:193], v[34:37]
	v_mfma_i32_16x16x64_i8 v[54:57], v[138:141], v[198:201], v[54:57]
	v_mfma_i32_16x16x64_i8 v[102:105], v[130:133], v[198:201], v[102:105]
	v_mfma_i32_16x16x64_i8 v[114:117], v[130:133], v[206:209], v[114:117]
	v_mfma_i32_16x16x64_i8 v[86:89], v[138:141], v[206:209], v[86:89]
	v_mfma_i32_16x16x64_i8 v[110:113], v[138:141], v[214:217], v[110:113]
	v_mfma_i32_16x16x64_i8 v[126:129], v[130:133], v[214:217], v[126:129]
	v_mfma_i32_16x16x64_i8 v[70:73], v[134:137], v[194:197], v[70:73]
	v_mfma_i32_16x16x64_i8 v[34:37], v[142:145], v[194:197], v[34:37]
	v_mfma_i32_16x16x64_i8 v[54:57], v[142:145], v[202:205], v[54:57]
	v_mfma_i32_16x16x64_i8 v[102:105], v[134:137], v[202:205], v[102:105]
	v_mfma_i32_16x16x64_i8 v[114:117], v[134:137], v[210:213], v[114:117]
	v_mfma_i32_16x16x64_i8 v[86:89], v[142:145], v[210:213], v[86:89]
	v_mfma_i32_16x16x64_i8 v[110:113], v[142:145], v[218:221], v[110:113]
	v_mfma_i32_16x16x64_i8 v[126:129], v[134:137], v[218:221], v[126:129]
	v_mfma_i32_16x16x64_i8 v[18:21], v[146:149], v[190:193], v[18:21]
	v_mfma_i32_16x16x64_i8 v[2:5], v[154:157], v[190:193], v[2:5]
	v_mfma_i32_16x16x64_i8 v[6:9], v[154:157], v[198:201], v[6:9]
	v_mfma_i32_16x16x64_i8 v[38:41], v[146:149], v[198:201], v[38:41]
	v_mfma_i32_16x16x64_i8 v[66:69], v[146:149], v[206:209], v[66:69]
	v_mfma_i32_16x16x64_i8 v[26:29], v[154:157], v[206:209], v[26:29]
	v_mfma_i32_16x16x64_i8 v[50:53], v[154:157], v[214:217], v[50:53]
	v_mfma_i32_16x16x64_i8 v[90:93], v[146:149], v[214:217], v[90:93]
	v_mfma_i32_16x16x64_i8 v[18:21], v[150:153], v[194:197], v[18:21]
	v_mfma_i32_16x16x64_i8 v[2:5], v[158:161], v[194:197], v[2:5]
	v_mfma_i32_16x16x64_i8 v[6:9], v[158:161], v[202:205], v[6:9]
	v_mfma_i32_16x16x64_i8 v[38:41], v[150:153], v[202:205], v[38:41]
	v_mfma_i32_16x16x64_i8 v[66:69], v[150:153], v[210:213], v[66:69]
	v_mfma_i32_16x16x64_i8 v[26:29], v[158:161], v[210:213], v[26:29]
	v_mfma_i32_16x16x64_i8 v[50:53], v[158:161], v[218:221], v[50:53]
	v_mfma_i32_16x16x64_i8 v[90:93], v[150:153], v[218:221], v[90:93]
	s_setprio 0
	s_barrier
	s_add_i32 s40, s65, s42
	s_mov_b32 m0, s40
	s_add_u32 s98, s8, 0x80
	s_addc_u32 s99, s9, 0
	ds_read_b128 v[190:193], v188 offset:49152
	ds_read_b128 v[194:197], v188 offset:50176
	ds_read_b128 v[198:201], v188 offset:51200
	ds_read_b128 v[202:205], v188 offset:52224
	ds_read_b128 v[206:209], v188 offset:53248
	ds_read_b128 v[210:213], v188 offset:54272
	ds_read_b128 v[214:217], v188 offset:55296
	ds_read_b128 v[218:221], v188 offset:56320
	global_load_lds_dwordx4 v162, s[98:99]
	s_add_i32 m0, s40, 0x2000
	s_add_u32 s8, s8, 0x80080
	s_addc_u32 s9, s9, 0
	s_add_i32 s40, s68, s42
	global_load_lds_dwordx4 v166, s[98:99]
	s_mov_b32 m0, s40
	s_nop 0
	global_load_lds_dwordx4 v162, s[8:9]
	s_add_i32 m0, s40, 0x2000
	s_nop 0
	global_load_lds_dwordx4 v166, s[8:9]
	s_mov_b32 m0, s66
	s_nop 0
	global_load_lds_dwordx4 v162, s[100:101]
	s_mov_b32 m0, s67
	s_nop 0
	global_load_lds_dwordx4 v166, s[100:101]
	s_waitcnt vmcnt(8) lgkmcnt(0)
	s_barrier
	s_setprio 1
	v_mfma_i32_16x16x64_i8 v[122:125], v[130:133], v[190:193], v[122:125]
	v_mfma_i32_16x16x64_i8 v[118:121], v[138:141], v[190:193], v[118:121]
	v_mfma_i32_16x16x64_i8 v[94:97], v[138:141], v[198:201], v[94:97]
	v_mfma_i32_16x16x64_i8 v[98:101], v[130:133], v[198:201], v[98:101]
	v_mfma_i32_16x16x64_i8 v[62:65], v[130:133], v[206:209], v[62:65]
	v_mfma_i32_16x16x64_i8 v[58:61], v[138:141], v[206:209], v[58:61]
	v_mfma_i32_16x16x64_i8 v[22:25], v[138:141], v[214:217], v[22:25]
	v_mfma_i32_16x16x64_i8 v[30:33], v[130:133], v[214:217], v[30:33]
	v_mfma_i32_16x16x64_i8 v[122:125], v[134:137], v[194:197], v[122:125]
	v_mfma_i32_16x16x64_i8 v[118:121], v[142:145], v[194:197], v[118:121]
	v_mfma_i32_16x16x64_i8 v[94:97], v[142:145], v[202:205], v[94:97]
	v_mfma_i32_16x16x64_i8 v[98:101], v[134:137], v[202:205], v[98:101]
	v_mfma_i32_16x16x64_i8 v[62:65], v[134:137], v[210:213], v[62:65]
	v_mfma_i32_16x16x64_i8 v[58:61], v[142:145], v[210:213], v[58:61]
	v_mfma_i32_16x16x64_i8 v[22:25], v[142:145], v[218:221], v[22:25]
	v_mfma_i32_16x16x64_i8 v[30:33], v[134:137], v[218:221], v[30:33]
	v_mfma_i32_16x16x64_i8 v[106:109], v[146:149], v[190:193], v[106:109]
	v_mfma_i32_16x16x64_i8 v[82:85], v[154:157], v[190:193], v[82:85]
	v_mfma_i32_16x16x64_i8 v[74:77], v[154:157], v[198:201], v[74:77]
	v_mfma_i32_16x16x64_i8 v[78:81], v[146:149], v[198:201], v[78:81]
	v_mfma_i32_16x16x64_i8 v[46:49], v[146:149], v[206:209], v[46:49]
	v_mfma_i32_16x16x64_i8 v[42:45], v[154:157], v[206:209], v[42:45]
	v_mfma_i32_16x16x64_i8 v[10:13], v[154:157], v[214:217], v[10:13]
	v_mfma_i32_16x16x64_i8 v[14:17], v[146:149], v[214:217], v[14:17]
	v_mfma_i32_16x16x64_i8 v[106:109], v[150:153], v[194:197], v[106:109]
	v_mfma_i32_16x16x64_i8 v[82:85], v[158:161], v[194:197], v[82:85]
	v_mfma_i32_16x16x64_i8 v[74:77], v[158:161], v[202:205], v[74:77]
	v_mfma_i32_16x16x64_i8 v[78:81], v[150:153], v[202:205], v[78:81]
	v_mfma_i32_16x16x64_i8 v[46:49], v[150:153], v[210:213], v[46:49]
	v_mfma_i32_16x16x64_i8 v[42:45], v[158:161], v[210:213], v[42:45]
	v_mfma_i32_16x16x64_i8 v[10:13], v[158:161], v[218:221], v[10:13]
	v_mfma_i32_16x16x64_i8 v[14:17], v[150:153], v[218:221], v[14:17]
	s_setprio 0
	s_barrier
	s_add_i32 s64, s64, 2
	s_add_u32 s6, s6, 0x100
	s_addc_u32 s7, s7, 0
	s_cmp_gt_u32 s64, 29
	s_cbranch_scc0 .LBB0_1051
	s_waitcnt vmcnt(0)
	s_cmpk_lt_u32 s59, 0x100
	s_cbranch_scc0 .LBB0_1054
	s_barrier

.LBB0_1173:
	ds_read_b128 v[158:161], v184
	ds_read_b128 v[150:153], v184 offset:1024
	ds_read_b128 v[154:157], v184 offset:2048
	ds_read_b128 v[146:149], v184 offset:3072
	ds_read_b128 v[142:145], v185
	ds_read_b128 v[130:133], v185 offset:1024
	ds_read_b128 v[138:141], v185 offset:2048
	ds_read_b128 v[134:137], v185 offset:3072
	s_add_u32 s38, s36, 0xfff80080
	s_addc_u32 s39, s37, -1
	s_cmp_eq_u32 s65, 28
	s_cselect_b32 s41, s18, s39
	s_cselect_b32 s40, s19, s38
	s_cselect_b32 s39, s25, s64
	s_cselect_b32 s38, s27, s63
	v_lshl_add_u64 v[212:213], s[36:37], 0, v[166:167]
	s_add_i32 m0, s35, 0xc000
	ds_read_b128 v[174:177], v186
	ds_read_b128 v[178:181], v186 offset:1024
	ds_read_b128 v[188:191], v186 offset:2048
	ds_read_b128 v[192:195], v186 offset:3072
	ds_read_b128 v[196:199], v186 offset:4096
	ds_read_b128 v[200:203], v186 offset:5120
	ds_read_b128 v[204:207], v186 offset:6144
	ds_read_b128 v[208:211], v186 offset:7168
	global_load_lds_dwordx4 v[212:213], off
	v_lshl_add_u64 v[212:213], s[36:37], 0, v[168:169]
	s_add_i32 m0, s35, 0xe000
	s_nop 0
	global_load_lds_dwordx4 v[212:213], off
	s_waitcnt vmcnt(8) lgkmcnt(0)
	s_barrier
	s_setprio 1
	v_mfma_i32_16x16x64_i8 v[126:129], v[158:161], v[174:177], v[126:129]
	v_mfma_i32_16x16x64_i8 v[122:125], v[154:157], v[174:177], v[122:125]
	v_mfma_i32_16x16x64_i8 v[106:109], v[154:157], v[188:191], v[106:109]
	v_mfma_i32_16x16x64_i8 v[110:113], v[158:161], v[188:191], v[110:113]
	v_mfma_i32_16x16x64_i8 v[94:97], v[158:161], v[196:199], v[94:97]
	v_mfma_i32_16x16x64_i8 v[90:93], v[154:157], v[196:199], v[90:93]
	v_mfma_i32_16x16x64_i8 v[74:77], v[154:157], v[204:207], v[74:77]
	v_mfma_i32_16x16x64_i8 v[78:81], v[158:161], v[204:207], v[78:81]
	v_mfma_i32_16x16x64_i8 v[126:129], v[150:153], v[178:181], v[126:129]
	v_mfma_i32_16x16x64_i8 v[122:125], v[146:149], v[178:181], v[122:125]
	v_mfma_i32_16x16x64_i8 v[106:109], v[146:149], v[192:195], v[106:109]
	v_mfma_i32_16x16x64_i8 v[110:113], v[150:153], v[192:195], v[110:113]
	v_mfma_i32_16x16x64_i8 v[94:97], v[150:153], v[200:203], v[94:97]
	v_mfma_i32_16x16x64_i8 v[90:93], v[146:149], v[200:203], v[90:93]
	v_mfma_i32_16x16x64_i8 v[74:77], v[146:149], v[208:211], v[74:77]
	v_mfma_i32_16x16x64_i8 v[78:81], v[150:153], v[208:211], v[78:81]
	v_mfma_i32_16x16x64_i8 v[118:121], v[142:145], v[174:177], v[118:121]
	v_mfma_i32_16x16x64_i8 v[114:117], v[138:141], v[174:177], v[114:117]
	v_mfma_i32_16x16x64_i8 v[98:101], v[138:141], v[188:191], v[98:101]
	v_mfma_i32_16x16x64_i8 v[102:105], v[142:145], v[188:191], v[102:105]
	v_mfma_i32_16x16x64_i8 v[86:89], v[142:145], v[196:199], v[86:89]
	v_mfma_i32_16x16x64_i8 v[82:85], v[138:141], v[196:199], v[82:85]
	v_mfma_i32_16x16x64_i8 v[66:69], v[138:141], v[204:207], v[66:69]
	v_mfma_i32_16x16x64_i8 v[70:73], v[142:145], v[204:207], v[70:73]
	v_mfma_i32_16x16x64_i8 v[118:121], v[130:133], v[178:181], v[118:121]
	v_mfma_i32_16x16x64_i8 v[114:117], v[134:137], v[178:181], v[114:117]
	v_mfma_i32_16x16x64_i8 v[98:101], v[134:137], v[192:195], v[98:101]
	v_mfma_i32_16x16x64_i8 v[102:105], v[130:133], v[192:195], v[102:105]
	v_mfma_i32_16x16x64_i8 v[86:89], v[130:133], v[200:203], v[86:89]
	v_mfma_i32_16x16x64_i8 v[82:85], v[134:137], v[200:203], v[82:85]
	v_mfma_i32_16x16x64_i8 v[66:69], v[134:137], v[208:211], v[66:69]
	v_mfma_i32_16x16x64_i8 v[70:73], v[130:133], v[208:211], v[70:73]
	s_setprio 0
	s_barrier
	s_add_i32 s66, s51, s3
	v_lshl_add_u64 v[174:175], s[38:39], 0, v[164:165]
	s_mov_b32 m0, s66
	ds_read_b128 v[188:191], v186 offset:16384
	ds_read_b128 v[192:195], v186 offset:17408
	ds_read_b128 v[196:199], v186 offset:18432
	ds_read_b128 v[200:203], v186 offset:19456
	ds_read_b128 v[204:207], v186 offset:20480
	ds_read_b128 v[208:211], v186 offset:21504
	ds_read_b128 v[212:215], v186 offset:22528
	ds_read_b128 v[216:219], v186 offset:23552
	global_load_lds_dwordx4 v[174:175], off
	s_add_i32 m0, s66, 0x2000
	s_add_u32 s66, s38, 0x80000
	v_lshl_add_u64 v[176:177], s[38:39], 0, v[162:163]
	s_addc_u32 s67, s39, 0
	s_add_i32 s68, s58, s3
	global_load_lds_dwordx4 v[176:177], off
	v_lshl_add_u64 v[178:179], s[66:67], 0, v[164:165]
	s_mov_b32 m0, s68
	v_lshl_add_u64 v[180:181], s[40:41], 0, v[162:163]
	global_load_lds_dwordx4 v[178:179], off
	v_lshl_add_u64 v[178:179], s[66:67], 0, v[162:163]
	s_add_i32 m0, s68, 0x2000
	s_nop 0
	global_load_lds_dwordx4 v[178:179], off
	v_lshl_add_u64 v[178:179], s[40:41], 0, v[164:165]
	s_mov_b32 m0, s35
	s_nop 0
	global_load_lds_dwordx4 v[178:179], off
	s_mov_b32 m0, s42
	s_nop 0
	global_load_lds_dwordx4 v[180:181], off
	s_waitcnt vmcnt(8) lgkmcnt(0)
	s_barrier
	s_setprio 1
	v_mfma_i32_16x16x64_i8 v[62:65], v[158:161], v[188:191], v[62:65]
	v_mfma_i32_16x16x64_i8 v[58:61], v[154:157], v[188:191], v[58:61]
	v_mfma_i32_16x16x64_i8 v[42:45], v[154:157], v[196:199], v[42:45]
	v_mfma_i32_16x16x64_i8 v[46:49], v[158:161], v[196:199], v[46:49]
	v_mfma_i32_16x16x64_i8 v[30:33], v[158:161], v[204:207], v[30:33]
	v_mfma_i32_16x16x64_i8 v[26:29], v[154:157], v[204:207], v[26:29]
	v_mfma_i32_16x16x64_i8 v[10:13], v[154:157], v[212:215], v[10:13]
	v_mfma_i32_16x16x64_i8 v[14:17], v[158:161], v[212:215], v[14:17]
	v_mfma_i32_16x16x64_i8 v[62:65], v[150:153], v[192:195], v[62:65]
	v_mfma_i32_16x16x64_i8 v[58:61], v[146:149], v[192:195], v[58:61]
	v_mfma_i32_16x16x64_i8 v[42:45], v[146:149], v[200:203], v[42:45]
	v_mfma_i32_16x16x64_i8 v[46:49], v[150:153], v[200:203], v[46:49]
	v_mfma_i32_16x16x64_i8 v[30:33], v[150:153], v[208:211], v[30:33]
	v_mfma_i32_16x16x64_i8 v[26:29], v[146:149], v[208:211], v[26:29]
	v_mfma_i32_16x16x64_i8 v[10:13], v[146:149], v[216:219], v[10:13]
	v_mfma_i32_16x16x64_i8 v[14:17], v[150:153], v[216:219], v[14:17]
	v_mfma_i32_16x16x64_i8 v[54:57], v[142:145], v[188:191], v[54:57]
	v_mfma_i32_16x16x64_i8 v[50:53], v[138:141], v[188:191], v[50:53]
	v_mfma_i32_16x16x64_i8 v[34:37], v[138:141], v[196:199], v[34:37]
	v_mfma_i32_16x16x64_i8 v[38:41], v[142:145], v[196:199], v[38:41]
	v_mfma_i32_16x16x64_i8 v[22:25], v[142:145], v[204:207], v[22:25]
	v_mfma_i32_16x16x64_i8 v[18:21], v[138:141], v[204:207], v[18:21]
	v_mfma_i32_16x16x64_i8 v[2:5], v[138:141], v[212:215], v[2:5]
	v_mfma_i32_16x16x64_i8 v[6:9], v[142:145], v[212:215], v[6:9]
	v_mfma_i32_16x16x64_i8 v[54:57], v[130:133], v[192:195], v[54:57]
	v_mfma_i32_16x16x64_i8 v[50:53], v[134:137], v[192:195], v[50:53]
	v_mfma_i32_16x16x64_i8 v[34:37], v[134:137], v[200:203], v[34:37]
	v_mfma_i32_16x16x64_i8 v[38:41], v[130:133], v[200:203], v[38:41]
	v_mfma_i32_16x16x64_i8 v[22:25], v[130:133], v[208:211], v[22:25]
	v_mfma_i32_16x16x64_i8 v[18:21], v[134:137], v[208:211], v[18:21]
	v_mfma_i32_16x16x64_i8 v[2:5], v[134:137], v[216:219], v[2:5]
	v_mfma_i32_16x16x64_i8 v[6:9], v[130:133], v[216:219], v[6:9]
	s_setprio 0
	s_barrier
	s_add_i32 s66, 0, 0x18000
	s_add_i32 s67, 0, 0x1c000
	v_add_u32_e32 v142, s66, v182
	v_add_u32_e32 v158, s67, v182
	ds_read_b128 v[130:133], v142
	ds_read_b128 v[134:137], v142 offset:1024
	ds_read_b128 v[138:141], v142 offset:2048
	ds_read_b128 v[142:145], v142 offset:3072
	ds_read_b128 v[146:149], v158
	ds_read_b128 v[150:153], v158 offset:1024
	ds_read_b128 v[154:157], v158 offset:2048
	ds_read_b128 v[158:161], v158 offset:3072
	s_add_u32 s40, s40, 0x80000
	s_addc_u32 s41, s41, 0
	s_mov_b32 m0, s43
	v_lshl_add_u64 v[220:221], s[40:41], 0, v[164:165]
	ds_read_b128 v[188:191], v186 offset:32768
	ds_read_b128 v[192:195], v186 offset:33792
	ds_read_b128 v[196:199], v186 offset:34816
	ds_read_b128 v[200:203], v186 offset:35840
	ds_read_b128 v[204:207], v186 offset:36864
	ds_read_b128 v[208:211], v186 offset:37888
	ds_read_b128 v[212:215], v186 offset:38912
	ds_read_b128 v[216:219], v186 offset:39936
	global_load_lds_dwordx4 v[220:221], off
	v_lshl_add_u64 v[220:221], s[40:41], 0, v[162:163]
	s_mov_b32 m0, s44
	s_nop 0
	global_load_lds_dwordx4 v[220:221], off
	s_waitcnt vmcnt(8) lgkmcnt(0)
	s_barrier
	s_setprio 1
	v_mfma_i32_16x16x64_i8 v[126:129], v[130:133], v[188:191], v[126:129]
	v_mfma_i32_16x16x64_i8 v[122:125], v[138:141], v[188:191], v[122:125]
	v_mfma_i32_16x16x64_i8 v[106:109], v[138:141], v[196:199], v[106:109]
	v_mfma_i32_16x16x64_i8 v[110:113], v[130:133], v[196:199], v[110:113]
	v_mfma_i32_16x16x64_i8 v[94:97], v[130:133], v[204:207], v[94:97]
	v_mfma_i32_16x16x64_i8 v[90:93], v[138:141], v[204:207], v[90:93]
	v_mfma_i32_16x16x64_i8 v[74:77], v[138:141], v[212:215], v[74:77]
	v_mfma_i32_16x16x64_i8 v[78:81], v[130:133], v[212:215], v[78:81]
	v_mfma_i32_16x16x64_i8 v[126:129], v[134:137], v[192:195], v[126:129]
	v_mfma_i32_16x16x64_i8 v[122:125], v[142:145], v[192:195], v[122:125]
	v_mfma_i32_16x16x64_i8 v[106:109], v[142:145], v[200:203], v[106:109]
	v_mfma_i32_16x16x64_i8 v[110:113], v[134:137], v[200:203], v[110:113]
	v_mfma_i32_16x16x64_i8 v[94:97], v[134:137], v[208:211], v[94:97]
	v_mfma_i32_16x16x64_i8 v[90:93], v[142:145], v[208:211], v[90:93]
	v_mfma_i32_16x16x64_i8 v[74:77], v[142:145], v[216:219], v[74:77]
	v_mfma_i32_16x16x64_i8 v[78:81], v[134:137], v[216:219], v[78:81]
	v_mfma_i32_16x16x64_i8 v[118:121], v[146:149], v[188:191], v[118:121]
	v_mfma_i32_16x16x64_i8 v[114:117], v[154:157], v[188:191], v[114:117]
	v_mfma_i32_16x16x64_i8 v[98:101], v[154:157], v[196:199], v[98:101]
	v_mfma_i32_16x16x64_i8 v[102:105], v[146:149], v[196:199], v[102:105]
	v_mfma_i32_16x16x64_i8 v[86:89], v[146:149], v[204:207], v[86:89]
	v_mfma_i32_16x16x64_i8 v[82:85], v[154:157], v[204:207], v[82:85]
	v_mfma_i32_16x16x64_i8 v[66:69], v[154:157], v[212:215], v[66:69]
	v_mfma_i32_16x16x64_i8 v[70:73], v[146:149], v[212:215], v[70:73]
	v_mfma_i32_16x16x64_i8 v[118:121], v[150:153], v[192:195], v[118:121]
	v_mfma_i32_16x16x64_i8 v[114:117], v[158:161], v[192:195], v[114:117]
	v_mfma_i32_16x16x64_i8 v[98:101], v[158:161], v[200:203], v[98:101]
	v_mfma_i32_16x16x64_i8 v[102:105], v[150:153], v[200:203], v[102:105]
	v_mfma_i32_16x16x64_i8 v[86:89], v[150:153], v[208:211], v[86:89]
	v_mfma_i32_16x16x64_i8 v[82:85], v[158:161], v[208:211], v[82:85]
	v_mfma_i32_16x16x64_i8 v[66:69], v[158:161], v[216:219], v[66:69]
	v_mfma_i32_16x16x64_i8 v[70:73], v[150:153], v[216:219], v[70:73]
	s_setprio 0
	s_barrier
	s_add_i32 s40, s66, s3
	v_lshl_add_u64 v[174:175], v[174:175], 0, s[8:9]
	s_mov_b32 m0, s40
	ds_read_b128 v[188:191], v186 offset:49152
	ds_read_b128 v[192:195], v186 offset:50176
	ds_read_b128 v[196:199], v186 offset:51200
	ds_read_b128 v[200:203], v186 offset:52224
	ds_read_b128 v[204:207], v186 offset:53248
	ds_read_b128 v[208:211], v186 offset:54272
	ds_read_b128 v[212:215], v186 offset:55296
	ds_read_b128 v[216:219], v186 offset:56320
	global_load_lds_dwordx4 v[174:175], off
	s_add_i32 m0, s40, 0x2000
	s_add_u32 s38, s38, 0x80080
	v_lshl_add_u64 v[174:175], v[176:177], 0, s[8:9]
	s_addc_u32 s39, s39, 0
	s_add_i32 s40, s67, s3
	global_load_lds_dwordx4 v[174:175], off
	v_lshl_add_u64 v[174:175], s[38:39], 0, v[164:165]
	s_mov_b32 m0, s40
	s_nop 0
	global_load_lds_dwordx4 v[174:175], off
	v_lshl_add_u64 v[174:175], s[38:39], 0, v[162:163]
	s_add_i32 m0, s40, 0x2000
	s_nop 0
	global_load_lds_dwordx4 v[174:175], off
	v_lshl_add_u64 v[174:175], v[178:179], 0, s[8:9]
	s_mov_b32 m0, s49
	s_nop 0
	global_load_lds_dwordx4 v[174:175], off
	v_lshl_add_u64 v[174:175], v[180:181], 0, s[8:9]
	s_mov_b32 m0, s50
	s_nop 0
	global_load_lds_dwordx4 v[174:175], off
	s_waitcnt vmcnt(8) lgkmcnt(0)
	s_barrier
	s_setprio 1
	v_mfma_i32_16x16x64_i8 v[62:65], v[130:133], v[188:191], v[62:65]
	v_mfma_i32_16x16x64_i8 v[58:61], v[138:141], v[188:191], v[58:61]
	v_mfma_i32_16x16x64_i8 v[42:45], v[138:141], v[196:199], v[42:45]
	v_mfma_i32_16x16x64_i8 v[46:49], v[130:133], v[196:199], v[46:49]
	v_mfma_i32_16x16x64_i8 v[30:33], v[130:133], v[204:207], v[30:33]
	v_mfma_i32_16x16x64_i8 v[26:29], v[138:141], v[204:207], v[26:29]
	v_mfma_i32_16x16x64_i8 v[10:13], v[138:141], v[212:215], v[10:13]
	v_mfma_i32_16x16x64_i8 v[14:17], v[130:133], v[212:215], v[14:17]
	v_mfma_i32_16x16x64_i8 v[62:65], v[134:137], v[192:195], v[62:65]
	v_mfma_i32_16x16x64_i8 v[58:61], v[142:145], v[192:195], v[58:61]
	v_mfma_i32_16x16x64_i8 v[42:45], v[142:145], v[200:203], v[42:45]
	v_mfma_i32_16x16x64_i8 v[46:49], v[134:137], v[200:203], v[46:49]
	v_mfma_i32_16x16x64_i8 v[30:33], v[134:137], v[208:211], v[30:33]
	v_mfma_i32_16x16x64_i8 v[26:29], v[142:145], v[208:211], v[26:29]
	v_mfma_i32_16x16x64_i8 v[10:13], v[142:145], v[216:219], v[10:13]
	v_mfma_i32_16x16x64_i8 v[14:17], v[134:137], v[216:219], v[14:17]
	v_mfma_i32_16x16x64_i8 v[54:57], v[146:149], v[188:191], v[54:57]
	v_mfma_i32_16x16x64_i8 v[50:53], v[154:157], v[188:191], v[50:53]
	v_mfma_i32_16x16x64_i8 v[34:37], v[154:157], v[196:199], v[34:37]
	v_mfma_i32_16x16x64_i8 v[38:41], v[146:149], v[196:199], v[38:41]
	v_mfma_i32_16x16x64_i8 v[22:25], v[146:149], v[204:207], v[22:25]
	v_mfma_i32_16x16x64_i8 v[18:21], v[154:157], v[204:207], v[18:21]
	v_mfma_i32_16x16x64_i8 v[2:5], v[154:157], v[212:215], v[2:5]
	v_mfma_i32_16x16x64_i8 v[6:9], v[146:149], v[212:215], v[6:9]
	v_mfma_i32_16x16x64_i8 v[54:57], v[150:153], v[192:195], v[54:57]
	v_mfma_i32_16x16x64_i8 v[50:53], v[158:161], v[192:195], v[50:53]
	v_mfma_i32_16x16x64_i8 v[34:37], v[158:161], v[200:203], v[34:37]
	v_mfma_i32_16x16x64_i8 v[38:41], v[150:153], v[200:203], v[38:41]
	v_mfma_i32_16x16x64_i8 v[22:25], v[150:153], v[208:211], v[22:25]
	v_mfma_i32_16x16x64_i8 v[18:21], v[158:161], v[208:211], v[18:21]
	v_mfma_i32_16x16x64_i8 v[2:5], v[158:161], v[216:219], v[2:5]
	v_mfma_i32_16x16x64_i8 v[6:9], v[150:153], v[216:219], v[6:9]
	s_setprio 0
	s_barrier
	s_add_i32 s65, s65, 2
	s_add_u32 s36, s36, 0x100
	s_addc_u32 s37, s37, 0
	s_add_u32 s63, s63, 0x100
	s_addc_u32 s64, s64, 0
	s_cmp_gt_u32 s65, 29
	s_cbranch_scc0 .LBB0_1173
	s_and_b64 vcc, exec, s[12:13]
	s_cbranch_vccz .LBB0_1176
	s_barrier
